# next-unit prefetch extended: the next unit's first weight tile B(0) is also loaded during the epilogue (into the dead staging registers) and copied in by the next prologue
# baseline (speedup 1.0000x reference)
; #define G_DMA_A(buf, t, i_) __builtin_amdgcn_raw_ptr_buffer_load_lds(ra, (LAS void*)(lds + (buf) * 65536 + a_wu + (i_) * 8192), 16, ao##i_, (unsigned)(t) * 128u, 0, 0)
; #define G_ISSUE_B(t) do { const unsigned so_ = (unsigned)(t) * 64u * ldbB; _Pragma("unroll") for (int i_ = 0; i_ < 8; ++i_) sb[i_] = __builtin_bit_cast(f32x4, __builtin_amdgcn_raw_buffer_load_b128(rb, bo, so_ + (unsigned)i_ * ldbB, 0)); } while (0)
; #define G_RETIRE() asm volatile("s_waitcnt vmcnt(0)" : "+v"(sb[0]), "+v"(sb[1]), "+v"(sb[2]), "+v"(sb[3]), "+v"(sb[4]), "+v"(sb[5]), "+v"(sb[6]), "+v"(sb[7]) :: "memory")
; #define G_WRITE_B(buf) do { LAS unsigned char* d_ = lds + (buf) * 65536; \
;         _Pragma("unroll") for (int j_ = 0; j_ < 4; ++j_) { u32x4 w_; w_.x = cvtpk(sb[0][j_], sb[1][j_]); w_.y = cvtpk(sb[2][j_], sb[3][j_]); w_.z = cvtpk(sb[4][j_], sb[5][j_]); w_.w = cvtpk(sb[6][j_], sb[7][j_]); \
;             *(LAS u32x4*)(d_ + 32768 + T.b_w + ((T.b_rot + 64u * j_) & 255u)) = w_; } } while (0)
; #define G_DMA_A(buf, t, i_) __builtin_amdgcn_raw_ptr_buffer_load_lds(ra, (LAS void*)(lds + (buf) * 65536 + a_wu + (i_) * 8192), 16, ao##i_, (unsigned)(t) * 128u, 0, 0)
; #define G_ISSUE_B(t) do { const unsigned so_ = (unsigned)(t) * 64u * ldbB; _Pragma("unroll") for (int i_ = 0; i_ < 8; ++i_) sb[i_] = __builtin_bit_cast(f32x4, __builtin_amdgcn_raw_buffer_load_b128(rb, bo, so_ + (unsigned)i_ * ldbB, 0)); } while (0)
; #define G_RETIRE() asm volatile("s_waitcnt vmcnt(0)" : "+v"(sb[0]), "+v"(sb[1]), "+v"(sb[2]), "+v"(sb[3]), "+v"(sb[4]), "+v"(sb[5]), "+v"(sb[6]), "+v"(sb[7]) :: "memory")
; __device__ __forceinline__ void gemm_kloop(f32x4 (&acc)[8][4], LAS unsigned char* lds, const GemmT& T, ...
;     ...
;     G_ISSUE_B(0); G_DMA_A(0, 0, 0); G_DMA_A(0, 0, 1); G_DMA_A(0, 0, 2); G_DMA_A(0, 0, 3); G_RETIRE(); G_WRITE_B(0);
; __device__ __forceinline__ void phase_moe_gu(const Ptrs& p, LAS unsigned char* lds) {
;     ...
;         for (int i = 0; i < 4; ++i) { const int r = i0 + T.aR + 64 * i; const int tok = (r < mu.cnt) ? (list[r] >> 2) : 0; ao[i] = (unsigned)((tok * D + T.aC) * 2); }
;         const float* wsel = ((__builtin_amdgcn_readfirstlane(T.b_p) & 1) ? p.w_up : p.w_gate) + (size_t)mu.e * D * D + n0;
;         const unsigned bo = (unsigned)((T.b_k * D + T.b_gucol) * 4);
.Lmy_pf_done:
	v_ashrrev_i32_e32 v5, 6, v3
	v_and_b32_e32 v11, 1, v5
	s_lshl_b32 s0, s85, 7
	v_readfirstlane_b32 s1, v11
	v_readlane_b32 s4, v246, 0
	s_bitcmp0_b32 s1, 0
	v_readlane_b32 s5, v246, 1
	s_cselect_b32 s1, s49, s5
	s_cselect_b32 s3, s48, s4
	s_lshl_b64 s[4:5], s[42:43], 24
	v_readlane_b32 s6, v246, 2
	s_add_u32 s3, s3, s4
	v_and_b32_e32 v4, 63, v3
	s_addc_u32 s6, s1, s5
	s_ashr_i32 s1, s0, 31
	v_lshrrev_b32_e32 v12, 5, v4
	v_bfe_u32 v13, v3, 1, 2
	s_lshl_b64 s[4:5], s[0:1], 2
	v_lshl_or_b32 v10, v10, 1, v12
	v_bfe_u32 v12, v3, 3, 2
	v_and_b32_e32 v14, 1, v3
	v_lshlrev_b32_e32 v15, 5, v13
	s_add_u32 s24, s3, s4
	v_lshl_or_b32 v15, v12, 7, v15
	v_lshlrev_b32_e32 v16, 16, v10
	v_lshlrev_b32_e32 v17, 4, v14
	s_addc_u32 s1, s6, s5
	v_or3_b32 v225, v15, v17, v16
	s_and_b32 s25, s1, 0xffff
	s_movk_i32 s1, 0x2000
	s_cmp_lg_u32 s98, 0
	s_cbranch_scc1 .Lmy_pf_b0use
	buffer_load_dwordx4 v[114:117], v225, s[24:27], 0 offen
	buffer_load_dwordx4 v[118:121], v225, s[24:27], s66 offen
	s_mov_b32 s3, 0x8000
	buffer_load_dwordx4 v[126:129], v225, s[24:27], s1 offen
	buffer_load_dwordx4 v[122:125], v225, s[24:27], s3 offen
	s_movk_i32 s1, 0x4000
	s_mov_b32 s3, 0xa000
	buffer_load_dwordx4 v[130:133], v225, s[24:27], s1 offen
	buffer_load_dwordx4 v[134:137], v225, s[24:27], s3 offen
	s_mov_b32 s1, 0xc000
	s_mov_b32 s3, 0xe000
	buffer_load_dwordx4 v[142:145], v225, s[24:27], s1 offen
	buffer_load_dwordx4 v[146:149], v225, s[24:27], s3 offen
	s_branch .Lmy_pf_b0done
.Lmy_pf_b0use:
	v_mov_b32_e32 v114, v162
	v_mov_b32_e32 v115, v163
	v_mov_b32_e32 v116, v164
	v_mov_b32_e32 v117, v165
	v_mov_b32_e32 v118, v166
	v_mov_b32_e32 v119, v167
	v_mov_b32_e32 v120, v168
	v_mov_b32_e32 v121, v169
	v_mov_b32_e32 v126, v170
	v_mov_b32_e32 v127, v171
	v_mov_b32_e32 v128, v172
	v_mov_b32_e32 v129, v173
	v_mov_b32_e32 v122, v174
	v_mov_b32_e32 v123, v175
	v_mov_b32_e32 v124, v176
	v_mov_b32_e32 v125, v177
	v_mov_b32_e32 v130, v178
	v_mov_b32_e32 v131, v179
	v_mov_b32_e32 v132, v180
	v_mov_b32_e32 v133, v181
	v_mov_b32_e32 v134, v182
	v_mov_b32_e32 v135, v183
	v_mov_b32_e32 v136, v184
	v_mov_b32_e32 v137, v185
	v_mov_b32_e32 v142, v186
	v_mov_b32_e32 v143, v187
	v_mov_b32_e32 v144, v188
	v_mov_b32_e32 v145, v189
	v_mov_b32_e32 v146, v190
	v_mov_b32_e32 v147, v191
	v_mov_b32_e32 v148, v192
	v_mov_b32_e32 v149, v193
.Lmy_pf_b0done:
	s_cmp_lg_u32 s98, 0
	s_cbranch_scc1 .Lmy_pf_fin
	s_waitcnt vmcnt(8)
	v_lshlrev_b32_e32 v7, 10, v7
	v_and_b32_e32 v7, 0xfffff000, v7
	v_lshlrev_b32_e32 v6, 10, v6
	v_and_b32_e32 v6, 0xfffff000, v6
	v_lshlrev_b32_e32 v9, 10, v9
	v_and_b32_e32 v9, 0xfffff000, v9
	v_lshlrev_b32_e32 v8, 10, v8
	v_and_b32_e32 v8, 0xfffff000, v8

; __device__ __forceinline__ bool moe_unit(int cv, int u, int ntiles_n, MoeUnit& mu) {
;     int base = 0;
; #pragma unroll
;     for (int e = 0; e < E; ++e) { const int c = __builtin_amdgcn_readlane(cv, e), tm = (c + 255) >> 8, nu = tm * ntiles_n;
;         if (u < nu) { mu.e = e; mu.cnt = c; mu.base = base; mu.nt = u / tm; mu.mt = u - mu.nt * tm; mu.light = (mu.mt == tm - 1 && c - mu.mt * 256 <= 128) ? 1 : 0; return true; }
;         u -= nu; base += tm * 256; }
;     return false;
; }
; __device__ __forceinline__ void phase_moe_gu(const Ptrs& p, LAS unsigned char* lds) {
;     ...
;         const float* wsel = ((__builtin_amdgcn_readfirstlane(T.b_p) & 1) ? p.w_up : p.w_gate) + (size_t)mu.e * D * D + n0;
;         const unsigned bo = (unsigned)((T.b_k * D + T.b_gucol) * 4);
.Lmy_pf_found:
	s_mov_b32 vcc_hi, 0
.Lmy_pf_mod:
	s_cmp_lt_i32 s98, s101
	s_cbranch_scc1 .Lmy_pf_mt
	s_sub_i32 s98, s98, s101
	s_add_i32 vcc_hi, vcc_hi, 1
	s_branch .Lmy_pf_mod
.Lmy_pf_mt:
	s_lshl_b32 s101, vcc_hi, 8
	s_or_b32 s101, s101, s99
	s_lshl_b32 vcc_lo, s99, 15
	s_add_u32 vcc_lo, s52, vcc_lo
	s_addc_u32 vcc_hi, s53, 0
	v_mov_b32_e32 v252, vcc_lo
	v_mov_b32_e32 v253, vcc_hi
	v_bfe_u32 v254, v0, 2, 4
	v_ashrrev_i32_e32 v251, 7, v0
	v_lshl_add_u32 v254, v251, 4, v254
	v_mov_b32_e32 v255, s98
	v_lshl_or_b32 v254, v255, 8, v254
	v_mov_b32_e32 v255, 0
	v_lshl_add_u64 v[252:253], v[254:255], 2, v[252:253]
	v_mov_b32_e32 v247, 0
	v_mov_b32_e32 v248, 0
	v_mov_b32_e32 v249, 0
	v_mov_b32_e32 v250, 0
	v_cmp_gt_i32_e32 vcc, s100, v254
	s_and_saveexec_b64 s[98:99], vcc
	global_load_dword v247, v[252:253], off
	s_or_b64 exec, exec, s[98:99]
	v_add_u32_e32 v251, 64, v254
	v_cmp_gt_i32_e32 vcc, s100, v251
	s_and_saveexec_b64 s[98:99], vcc
	global_load_dword v248, v[252:253], off offset:256
	s_or_b64 exec, exec, s[98:99]
	v_add_u32_e32 v251, 128, v254
	v_cmp_gt_i32_e32 vcc, s100, v251
	s_and_saveexec_b64 s[98:99], vcc
	global_load_dword v249, v[252:253], off offset:512
	s_or_b64 exec, exec, s[98:99]
	v_add_u32_e32 v251, 192, v254
	v_cmp_gt_i32_e32 vcc, s100, v251
	s_and_saveexec_b64 s[98:99], vcc
	global_load_dword v250, v[252:253], off offset:768
	s_or_b64 exec, exec, s[98:99]
	s_mov_b32 s98, 1
.Lmy_pf_none:
	v_or_b32_e32 v130, s0, v4
	s_lshl_b64 s[0:1], s[42:43], 13
	s_add_u32 s4, s50, s0
	v_ashrrev_i32_e32 v131, 31, v130
	s_addc_u32 s5, s51, s1
	v_lshlrev_b64 v[4:5], 2, v[130:131]
	v_lshl_add_u64 v[114:115], s[4:5], 0, v[4:5]
	v_readlane_b32 s4, v246, 0
	v_readlane_b32 s6, v246, 2
	v_readlane_b32 s7, v246, 3
	s_add_u32 s0, s6, s0
	s_addc_u32 s1, s7, s1
	v_lshl_add_u64 v[4:5], s[0:1], 0, v[4:5]
	global_load_dwordx4 v[126:129], v[114:115], off offset:16
	global_load_dwordx4 v[118:121], v[114:115], off
	s_nop 0
	global_load_dwordx4 v[114:117], v[4:5], off
	global_load_dwordx4 v[122:125], v[4:5], off offset:16
	v_ashrrev_i32_e32 v4, 1, v3
	v_and_b32_e32 v4, 0xffffff80, v4
	v_add_u32_e32 v4, s2, v4
	v_and_or_b32 v4, v3, 15, v4
	v_lshlrev_b32_e32 v3, 1, v130
	v_cmp_gt_i32_e32 vcc, s87, v4
	v_readlane_b32 s5, v246, 1
	v_readlane_b32 s8, v246, 4
	v_readlane_b32 s9, v246, 5
	v_readlane_b32 s10, v246, 6
	v_readlane_b32 s11, v246, 7
	s_waitcnt vmcnt(0)
	s_cmp_eq_u32 s98, 0
	s_cbranch_scc1 .Lmy_pf_nodma
	v_lshlrev_b32_e32 v247, 10, v247
	v_and_b32_e32 v247, 0xfffff000, v247
	v_lshlrev_b32_e32 v248, 10, v248
	v_and_b32_e32 v248, 0xfffff000, v248
	v_lshlrev_b32_e32 v249, 10, v249
	v_and_b32_e32 v249, 0xfffff000, v249
	v_lshlrev_b32_e32 v250, 10, v250
	v_and_b32_e32 v250, 0xfffff000, v250
	v_ashrrev_i32_e32 v251, 6, v0
	v_and_b32_e32 v251, 1, v251
	v_lshlrev_b32_e32 v252, 4, v0
	v_and_b32_e32 v252, 48, v252
	v_lshlrev_b32_e32 v251, 6, v251
	v_and_b32_e32 v253, 32, v0
	v_bitop3_b32 v251, v252, v251, v253 bitop3:0xde
	v_lshrrev_b32_e32 v252, 6, v0
	v_lshlrev_b32_e32 v252, 10, v252
	s_nop 1
	v_readfirstlane_b32 s100, v252
	s_mov_b32 s38, s26
	s_mov_b32 s39, s27
	v_or_b32_e32 v252, v247, v251
	s_mov_b32 m0, s100
	s_nop 0
	buffer_load_dwordx4 v252, s[36:39], 0 offen lds
	v_or_b32_e32 v253, v248, v251
	s_add_i32 m0, s100, 0x2000
	s_nop 0
	buffer_load_dwordx4 v253, s[36:39], 0 offen lds
	v_or_b32_e32 v254, v249, v251
	s_add_i32 m0, s100, 0x4000
	s_nop 0
	buffer_load_dwordx4 v254, s[36:39], 0 offen lds
	v_or_b32_e32 v255, v250, v251
	s_add_i32 m0, s100, 0x6000
	s_nop 0
	buffer_load_dwordx4 v255, s[36:39], 0 offen lds
	v_ashrrev_i32_e32 v251, 6, v0
	v_and_b32_e32 v251, 1, v251
	s_nop 1
	s_and_b32 s99, s101, 0xff
	s_lshr_b32 s100, s101, 8
	s_sub_i32 s99, s99, s42
	s_lshl_b32 s99, s99, 24
	s_sub_i32 s100, s100, s85
	s_lshl_b32 s100, s100, 9
	s_add_i32 s99, s99, s100
	s_ashr_i32 s100, s99, 31
	s_add_u32 s24, s24, s99
	s_addc_u32 s25, s25, s100
	s_and_b32 s25, s25, 0xffff
	v_mov_b32_e32 v252, s24
	v_mov_b32_e32 v253, s25
	v_and_b32_e32 v251, 63, v0
	v_lshrrev_b32_e32 v251, 5, v251
	v_ashrrev_i32_e32 v254, 7, v0
	v_lshl_or_b32 v254, v254, 1, v251
	v_lshlrev_b32_e32 v254, 16, v254
	v_bfe_u32 v251, v0, 3, 2
	v_lshlrev_b32_e32 v251, 7, v251
	v_or_b32_e32 v254, v254, v251
	v_bfe_u32 v251, v0, 1, 2
	v_lshlrev_b32_e32 v251, 5, v251
	v_or_b32_e32 v254, v254, v251
	v_and_b32_e32 v251, 1, v0
	v_lshlrev_b32_e32 v251, 4, v251
	v_or_b32_e32 v254, v254, v251
	v_mov_b32_e32 v255, 0
	v_lshl_add_u64 v[252:253], v[254:255], 0, v[252:253]
	s_mov_b32 s101, 0
	global_load_dwordx4 v[162:165], v[252:253], off
	s_mov_b32 s100, 0x6000
	v_lshl_add_u64 v[254:255], v[252:253], 0, s[100:101]
	global_load_dwordx4 v[166:169], v[254:255], off
	s_mov_b32 s100, 0x2000
	v_lshl_add_u64 v[254:255], v[252:253], 0, s[100:101]
	global_load_dwordx4 v[170:173], v[254:255], off
	s_mov_b32 s100, 0x8000
	v_lshl_add_u64 v[254:255], v[252:253], 0, s[100:101]
	global_load_dwordx4 v[174:177], v[254:255], off
	s_mov_b32 s100, 0x4000
	v_lshl_add_u64 v[254:255], v[252:253], 0, s[100:101]
	global_load_dwordx4 v[178:181], v[254:255], off
	s_mov_b32 s100, 0xa000
	v_lshl_add_u64 v[254:255], v[252:253], 0, s[100:101]
	global_load_dwordx4 v[182:185], v[254:255], off
	s_mov_b32 s100, 0xc000
	v_lshl_add_u64 v[254:255], v[252:253], 0, s[100:101]
	global_load_dwordx4 v[186:189], v[254:255], off
	s_mov_b32 s100, 0xe000
	v_lshl_add_u64 v[254:255], v[252:253], 0, s[100:101]
	global_load_dwordx4 v[190:193], v[254:255], off
